# NSA score copies eliminated + background conversion in the NSA tile loop, placement kept
# speedup vs baseline: 1.0086x; 1.0086x over previous
.LBB0_2419:
	s_lshl_b32 s2, s2, 13
	s_add_i32 s76, s2, 0
	s_add_i32 s76, s76, 0x10000
	s_andn2_b64 vcc, exec, s[8:9]
	v_lshlrev_b32_e32 v134, 2, v162
	s_cbranch_vccnz .LBB0_2468
	v_or_b32_e32 v6, 32, v168
	v_cmp_gt_i32_e64 s[40:41], v6, v2
	v_cmp_lt_i32_e64 s[42:43], v6, v2
	v_or_b32_e32 v6, 34, v168
	v_cmp_gt_i32_e64 s[44:45], v6, v2
	v_or_b32_e32 v6, 35, v168
	v_cmp_gt_i32_e64 s[46:47], v6, v2
	v_or_b32_e32 v6, 40, v168
	v_cmp_gt_i32_e64 s[48:49], v6, v2
	v_or_b32_e32 v6, 41, v168
	v_cmp_gt_i32_e64 s[50:51], v6, v2
	v_or_b32_e32 v6, 42, v168
	v_cmp_gt_i32_e64 s[52:53], v6, v2
	v_or_b32_e32 v6, 43, v168
	v_cmp_gt_i32_e64 s[54:55], v6, v2
	v_or_b32_e32 v6, 48, v168
	v_cmp_gt_i32_e64 s[56:57], v6, v2
	v_or_b32_e32 v6, 49, v168
	v_cmp_gt_i32_e64 s[58:59], v6, v2
	v_or_b32_e32 v6, 50, v168
	v_cmp_gt_i32_e64 s[60:61], v6, v2
	v_or_b32_e32 v6, 51, v168
	v_cmp_gt_i32_e64 s[62:63], v6, v2
	v_or_b32_e32 v6, 56, v168
	v_cmp_gt_i32_e64 s[64:65], v6, v2
	v_or_b32_e32 v6, 57, v168
	v_cmp_gt_i32_e64 s[66:67], v6, v2
	v_or_b32_e32 v6, 58, v168
	v_cmp_gt_i32_e64 s[68:69], v6, v2
	v_or_b32_e32 v6, 59, v168
	v_cmp_gt_i32_e64 s[6:7], v168, v2
	v_cmp_lt_i32_e64 s[8:9], v168, v2
	v_cmp_gt_i32_e64 s[10:11], v135, v2
	v_cmp_gt_i32_e64 s[12:13], v169, v2
	v_cmp_gt_i32_e64 s[14:15], v170, v2
	v_cmp_gt_i32_e64 s[16:17], v171, v2
	v_cmp_gt_i32_e64 s[18:19], v172, v2
	v_cmp_gt_i32_e64 s[20:21], v173, v2
	v_cmp_gt_i32_e64 s[22:23], v174, v2
	v_cmp_gt_i32_e64 s[24:25], v175, v2
	v_cmp_gt_i32_e64 s[26:27], v176, v2
	v_cmp_gt_i32_e64 s[28:29], v177, v2
	v_cmp_gt_i32_e64 s[30:31], v178, v2
	v_cmp_gt_i32_e64 s[34:35], v179, v2
	v_cmp_gt_i32_e64 s[36:37], v180, v2
	v_cmp_gt_i32_e64 s[38:39], v181, v2
	v_cmp_gt_i32_e64 s[70:71], v6, v2
	s_min_u32 s2, s92, 8
	v_lshlrev_b32_e32 v2, 4, v4
	s_add_i32 s2, s92, s2
	v_and_b32_e32 v2, 0xc0, v2
	s_lshl_b32 s87, s2, 13
	v_lshl_or_b32 v2, v160, 8, v2
	v_readlane_b32 s2, v247, 4
	v_lshlrev_b32_e32 v5, 1, v4
	v_mov_b32_e32 v140, 0
	v_add_u32_e32 v185, s2, v2
	v_readlane_b32 s2, v247, 5
	s_movk_i32 s96, 0xc00
	s_add_i32 s91, s91, s92
	v_add_u32_e32 v187, s2, v2
	v_readlane_b32 s2, v247, 6
	s_add_i32 s93, s93, s3
	v_mov_b32_e32 v139, v131
	v_add_u32_e32 v188, s2, v2
	v_readlane_b32 s2, v247, 7
	s_mov_b32 s94, 2
	v_add_u32_e32 v183, s75, v134
	v_add_u32_e32 v189, s2, v2
	v_readlane_b32 s2, v247, 8
	v_add3_u32 v184, s76, v166, v134
	s_lshl_b32 s95, s92, 13
	v_add_u32_e32 v190, s2, v2
	v_readlane_b32 s2, v247, 9
	s_addk_i32 s87, 0x4000
	v_and_or_b32 v186, v5, 32, v3
	v_add_u32_e32 v191, s2, v2
	v_readlane_b32 s2, v247, 10
	s_add_i32 s86, s75, 0xc000
	s_mov_b32 s3, 0
	v_add_u32_e32 v192, s2, v2
	v_readlane_b32 s2, v247, 11
	v_mov_b32_e32 v202, 0
	v_mov_b32_e32 v3, v140
	v_add_u32_e32 v193, s2, v2
	v_readlane_b32 s2, v247, 12
	v_mov_b32_e32 v4, v140
	v_mov_b32_e32 v5, v140
	v_add_u32_e32 v194, s2, v2
	v_readlane_b32 s2, v247, 13
	v_mov_b32_e32 v6, v140
	v_mov_b32_e32 v7, v140
	v_add_u32_e32 v195, s2, v2
	v_readlane_b32 s2, v247, 14
	v_mov_b32_e32 v8, v140
	v_mov_b32_e32 v9, v140
	v_add_u32_e32 v196, s2, v2
	v_readlane_b32 s2, v247, 15
	v_mov_b32_e32 v10, v140
	v_mov_b32_e32 v11, v140
	v_add_u32_e32 v197, s2, v2
	v_readlane_b32 s2, v247, 16
	v_mov_b32_e32 v12, v140
	v_mov_b32_e32 v13, v140
	v_add_u32_e32 v198, s2, v2
	v_readlane_b32 s2, v247, 17
	v_mov_b32_e32 v14, v140
	v_mov_b32_e32 v15, v140
	v_add_u32_e32 v199, s2, v2
	v_readlane_b32 s2, v247, 21
	v_mov_b32_e32 v16, v140
	v_mov_b32_e32 v17, v140
	v_add_u32_e32 v200, s2, v2
	s_add_i32 s2, 0, 0x8000
	v_add_u32_e32 v201, s2, v2
	s_mov_b32 s2, 0
	v_mov_b32_e32 v2, 0
	v_mov_b32_e32 v18, 0
	v_mov_b32_e32 v19, v140
	v_mov_b32_e32 v20, v140
	v_mov_b32_e32 v21, v140
	v_mov_b32_e32 v22, v140
	v_mov_b32_e32 v23, v140
	v_add_u32_e32 v226, v201, v186
	s_nop 0
	s_nop 0
	s_nop 0
	s_nop 0
	s_nop 0
	s_nop 0
	s_nop 0
	v_mov_b32_e32 v24, v140
	v_mov_b32_e32 v25, v140
	v_mov_b32_e32 v26, v140
	v_mov_b32_e32 v27, v140
	v_mov_b32_e32 v28, v140
	v_mov_b32_e32 v29, v140
	v_mov_b32_e32 v30, v140
	v_mov_b32_e32 v31, v140
	v_mov_b32_e32 v32, v140
	v_mov_b32_e32 v33, v140
	v_mov_b64_e32 v[50:51], v[98:99]
	v_mov_b64_e32 v[52:53], v[100:101]
	v_mov_b64_e32 v[54:55], v[102:103]
	v_mov_b64_e32 v[56:57], v[104:105]
	v_mov_b64_e32 v[58:59], v[106:107]
	v_mov_b64_e32 v[60:61], v[108:109]
	v_mov_b64_e32 v[62:63], v[110:111]
	v_mov_b64_e32 v[64:65], v[112:113]
	s_mov_b32 s32, 0
	v_readlane_b32 s72, v249, 50
	s_cmp_gt_i32 s72, 7
	s_cbranch_scc1 .LBB0_2422
	s_mul_i32 s72, s72, 48
	v_readlane_b32 s73, v248, 47
	s_add_i32 s72, s73, s72
	v_readlane_b32 s78, v248, 48
	s_add_i32 s73, s72, 48
	s_min_i32 s78, s78, s73
	s_min_i32 s78, s78, 0x1be90
	v_readlane_b32 s84, v249, 16
	s_add_i32 s73, s72, s84
	s_cmp_ge_i32 s73, s78
	s_cbranch_scc1 .LBB0_2422
	v_writelane_b32 v244, s78, 3
	s_lshl_b32 s84, s84, 11
	s_add_i32 s84, s84, 0x24000
	v_and_b32_e32 v82, 63, v0
	v_and_b32_e32 v83, 31, v82
	v_lshrrev_b32_e32 v84, 5, v82
	v_lshlrev_b32_e32 v84, 10, v84
	v_lshl_add_u32 v83, v83, 2, v84
	v_add_u32_e32 v245, s84, v83
	s_mov_b32 s85, 2
	s_mov_b32 s32, 0x30
	s_branch .Lbgn_dec

.Lbgn_dd:
	s_waitcnt lgkmcnt(0)
	s_add_u32 s98, s98, s101
	s_addc_u32 s99, s99, 0
	s_add_u32 s100, s78, s100
	s_addc_u32 s101, s79, 0
	s_and_b32 s72, s32, 1
	s_cmp_eq_u32 s72, s85
	s_cbranch_scc1 .Lbgn_same
	s_cmp_eq_u32 s72, 1
	s_cselect_b32 s97, 13, 11
	s_cselect_b32 s85, 9, 11
	s_mov_b32 s72, 0x8000
	s_cselect_b32 s72, 0x20000, s72
	v_and_b32_e32 v82, 63, v0
	v_lshrrev_b32_e32 v83, 3, v82
	v_and_b32_e32 v84, 7, v82
	v_lshlrev_b32_e32 v83, s97, v83
	v_lshl_add_u32 v83, v84, 4, v83
	v_and_b32_e32 v85, 31, v82
	v_lshrrev_b32_e32 v84, 5, v82
	v_lshlrev_b32_e32 v85, s85, v85
	v_lshl_add_u32 v85, v84, 3, v85
	v_lshl_or_b32 v246, v85, 16, v83
	v_writelane_b32 v244, s72, 5
	v_and_b32_e32 v84, 0xffff, v246
.Lbgn_same:
	v_readlane_b32 s72, v244, 5
	s_bitcmp1_b32 s32, 5
	s_cbranch_scc0 .Lbgn_issue
	s_mov_b32 m0, s84
	s_andn2_b32 s32, s32, 0x20
	global_load_lds_dwordx4 v84, s[98:99] nt
	s_branch .Lbgn_issue
	s_nop 0
	s_nop 0
	s_nop 0
	s_nop 0
	s_nop 0
	s_nop 0
	s_nop 0
	s_nop 0
	s_nop 0
	s_nop 0
	s_nop 0
	s_nop 0
	s_nop 0
	s_nop 0
	s_branch .LBB0_2422

.Lbgn_wd:
	ds_read2_b32 v[86:87], v245 offset1:32
	ds_read2_b32 v[88:89], v245 offset0:64 offset1:96
	ds_read2_b32 v[90:91], v245 offset0:128 offset1:160
	ds_read2_b32 v[92:93], v245 offset0:192 offset1:224
	v_lshrrev_b32_e32 v85, 16, v246
	v_and_b32_e32 v84, 0xffff, v246
	v_mov_b32_e32 v94, 0x42800000
	v_readlane_b32 s72, v244, 5
	v_readfirstlane_b32 s84, v245
	s_waitcnt lgkmcnt(0)
	v_pk_mul_f32 v[86:87], v[86:87], v[94:95] op_sel_hi:[1,0]
	v_pk_mul_f32 v[88:89], v[88:89], v[94:95] op_sel_hi:[1,0]
	v_pk_mul_f32 v[90:91], v[90:91], v[94:95] op_sel_hi:[1,0]
	v_pk_mul_f32 v[92:93], v[92:93], v[94:95] op_sel_hi:[1,0]
	v_cvt_pk_fp8_f32 v96, v86, v87
	v_cvt_pk_fp8_f32 v97, v90, v91
	v_cvt_pk_fp8_f32 v96, v88, v89 op_sel:[0,0,1]
	v_cvt_pk_fp8_f32 v97, v92, v93 op_sel:[0,0,1]
	s_addk_i32 s32, 0x100
	global_store_dwordx2 v85, v[96:97], s[100:101]
	s_add_u32 s100, s100, 16
	s_and_b32 s73, s100, 0x30
	s_cbranch_scc0 .Lbgn_new
	s_add_u32 s98, s98, s72
	s_addc_u32 s99, s99, 0
.Lbgn_issue:
	s_mov_b32 m0, s84
	s_lshr_b32 s72, s72, 1
	s_add_u32 s80, s98, s72
	s_addc_u32 s81, s99, 0
	global_load_lds_dwordx4 v84, s[98:99] nt
	s_add_i32 m0, m0, 0x400
	s_nop 0
	global_load_lds_dwordx4 v84, s[80:81] nt
